# ml_scan body hand-written: all 16 kv loads + gate loads of a block issued up front, counted vmcnt per step (was one load + vmcnt(0) per step); same math; on top of v48
# speedup vs baseline: 1.0154x; 1.0016x over previous
.LBB0_485:
	s_cmp_eq_u32 s13, 0
	s_cselect_b64 vcc, -1, 0
	v_add_u32_e32 v6, s13, v23
	v_cndmask_b32_e32 v6, v6, v22, vcc
	v_ashrrev_i32_e32 v7, 31, v6
	v_mad_i64_i32 v[8:9], s[14:15], v6, s8, v[14:15]
	v_lshl_add_u64 v[6:7], v[6:7], 2, s[0:1]
	global_load_dwordx2 v[36:37], v[8:9], off
	global_load_dword v10, v[6:7], off
	v_lshl_add_u64 v[20:21], s[54:55], 0, v[16:17]
	v_lshl_add_u64 v[6:7], s[54:55], 0, v[18:19]
	s_mov_b64 s[14:15], 0x1400000
	v_lshl_add_u64 v[6:7], v[6:7], 0, s[14:15]
	global_load_dwordx4 v[68:71], v[6:7], off
	global_load_dwordx4 v[72:75], v[6:7], off offset:16
	global_load_dwordx4 v[76:79], v[6:7], off offset:32
	global_load_dwordx3 v[80:82], v[6:7], off offset:48
	s_mov_b64 s[14:15], 0xae80000
	v_lshl_add_u64 v[38:39], v[20:21], 0, s[14:15]
	global_load_dwordx2 v[38:39], v[38:39], off
	s_mov_b64 s[14:15], 0xae91000
	v_lshl_add_u64 v[40:41], v[20:21], 0, s[14:15]
	global_load_dwordx2 v[40:41], v[40:41], off
	s_mov_b64 s[14:15], 0xaea2000
	v_lshl_add_u64 v[42:43], v[20:21], 0, s[14:15]
	global_load_dwordx2 v[42:43], v[42:43], off
	s_mov_b64 s[14:15], 0xaeb3000
	v_lshl_add_u64 v[44:45], v[20:21], 0, s[14:15]
	global_load_dwordx2 v[44:45], v[44:45], off
	s_mov_b64 s[14:15], 0xaec4000
	v_lshl_add_u64 v[46:47], v[20:21], 0, s[14:15]
	global_load_dwordx2 v[46:47], v[46:47], off
	s_mov_b64 s[14:15], 0xaed5000
	v_lshl_add_u64 v[48:49], v[20:21], 0, s[14:15]
	global_load_dwordx2 v[48:49], v[48:49], off
	s_mov_b64 s[14:15], 0xaee6000
	v_lshl_add_u64 v[50:51], v[20:21], 0, s[14:15]
	global_load_dwordx2 v[50:51], v[50:51], off
	s_mov_b64 s[14:15], 0xaef7000
	v_lshl_add_u64 v[52:53], v[20:21], 0, s[14:15]
	global_load_dwordx2 v[52:53], v[52:53], off
	s_mov_b64 s[14:15], 0xaf08000
	v_lshl_add_u64 v[54:55], v[20:21], 0, s[14:15]
	global_load_dwordx2 v[54:55], v[54:55], off
	s_mov_b64 s[14:15], 0xaf19000
	v_lshl_add_u64 v[56:57], v[20:21], 0, s[14:15]
	global_load_dwordx2 v[56:57], v[56:57], off
	s_mov_b64 s[14:15], 0xaf2a000
	v_lshl_add_u64 v[58:59], v[20:21], 0, s[14:15]
	global_load_dwordx2 v[58:59], v[58:59], off
	s_mov_b64 s[14:15], 0xaf3b000
	v_lshl_add_u64 v[60:61], v[20:21], 0, s[14:15]
	global_load_dwordx2 v[60:61], v[60:61], off
	s_mov_b64 s[14:15], 0xaf4c000
	v_lshl_add_u64 v[62:63], v[20:21], 0, s[14:15]
	global_load_dwordx2 v[62:63], v[62:63], off
	s_mov_b64 s[14:15], 0xaf5d000
	v_lshl_add_u64 v[64:65], v[20:21], 0, s[14:15]
	global_load_dwordx2 v[64:65], v[64:65], off
	s_mov_b64 s[14:15], 0xaf6e000
	v_lshl_add_u64 v[66:67], v[20:21], 0, s[14:15]
	global_load_dwordx2 v[66:67], v[66:67], off
	s_waitcnt vmcnt(19)
	v_mul_f32_e32 v10, 0x3fb8aa3b, v10
	v_exp_f32_e32 v10, v10
	v_lshlrev_b32_e32 v8, 16, v36
	v_and_b32_e32 v9, 0xffff0000, v36
	v_lshlrev_b32_e32 v32, 16, v37
	v_and_b32_e32 v33, 0xffff0000, v37
	v_pk_fma_f32 v[2:3], v[2:3], v[10:11], v[8:9] op_sel_hi:[1,0,1]
	v_pk_fma_f32 v[4:5], v[4:5], v[10:11], v[32:33] op_sel_hi:[1,0,1]
	s_mov_b64 s[14:15], 0x9d00000
	v_lshl_add_u64 v[8:9], v[20:21], 0, s[14:15]
	v_cvt_pk_bf16_f32 v6, v2, v3
	v_cvt_pk_bf16_f32 v7, v4, v5
	global_store_dwordx2 v[8:9], v[6:7], off sc1
	s_waitcnt vmcnt(15)
	v_mul_f32_e32 v68, 0x3fb8aa3b, v68
	v_exp_f32_e32 v10, v68
	v_lshlrev_b32_e32 v8, 16, v38
	v_and_b32_e32 v9, 0xffff0000, v38
	v_lshlrev_b32_e32 v32, 16, v39
	v_and_b32_e32 v33, 0xffff0000, v39
	v_pk_fma_f32 v[2:3], v[2:3], v[10:11], v[8:9] op_sel_hi:[1,0,1]
	v_pk_fma_f32 v[4:5], v[4:5], v[10:11], v[32:33] op_sel_hi:[1,0,1]
	s_mov_b64 s[14:15], 0x9d11000
	v_lshl_add_u64 v[8:9], v[20:21], 0, s[14:15]
	v_cvt_pk_bf16_f32 v6, v2, v3
	v_cvt_pk_bf16_f32 v7, v4, v5
	global_store_dwordx2 v[8:9], v[6:7], off sc1
	s_waitcnt vmcnt(15)
	v_mul_f32_e32 v69, 0x3fb8aa3b, v69
	v_exp_f32_e32 v10, v69
	v_lshlrev_b32_e32 v8, 16, v40
	v_and_b32_e32 v9, 0xffff0000, v40
	v_lshlrev_b32_e32 v32, 16, v41
	v_and_b32_e32 v33, 0xffff0000, v41
	v_pk_fma_f32 v[2:3], v[2:3], v[10:11], v[8:9] op_sel_hi:[1,0,1]
	v_pk_fma_f32 v[4:5], v[4:5], v[10:11], v[32:33] op_sel_hi:[1,0,1]
	s_mov_b64 s[14:15], 0x9d22000
	v_lshl_add_u64 v[8:9], v[20:21], 0, s[14:15]
	v_cvt_pk_bf16_f32 v6, v2, v3
	v_cvt_pk_bf16_f32 v7, v4, v5
	global_store_dwordx2 v[8:9], v[6:7], off sc1
	s_waitcnt vmcnt(15)
	v_mul_f32_e32 v70, 0x3fb8aa3b, v70
	v_exp_f32_e32 v10, v70
	v_lshlrev_b32_e32 v8, 16, v42
	v_and_b32_e32 v9, 0xffff0000, v42
	v_lshlrev_b32_e32 v32, 16, v43
	v_and_b32_e32 v33, 0xffff0000, v43
	v_pk_fma_f32 v[2:3], v[2:3], v[10:11], v[8:9] op_sel_hi:[1,0,1]
	v_pk_fma_f32 v[4:5], v[4:5], v[10:11], v[32:33] op_sel_hi:[1,0,1]
	s_mov_b64 s[14:15], 0x9d33000
	v_lshl_add_u64 v[8:9], v[20:21], 0, s[14:15]
	v_cvt_pk_bf16_f32 v6, v2, v3
	v_cvt_pk_bf16_f32 v7, v4, v5
	global_store_dwordx2 v[8:9], v[6:7], off sc1
	s_waitcnt vmcnt(15)
	v_mul_f32_e32 v71, 0x3fb8aa3b, v71
	v_exp_f32_e32 v10, v71
	v_lshlrev_b32_e32 v8, 16, v44
	v_and_b32_e32 v9, 0xffff0000, v44
	v_lshlrev_b32_e32 v32, 16, v45
	v_and_b32_e32 v33, 0xffff0000, v45
	v_pk_fma_f32 v[2:3], v[2:3], v[10:11], v[8:9] op_sel_hi:[1,0,1]
	v_pk_fma_f32 v[4:5], v[4:5], v[10:11], v[32:33] op_sel_hi:[1,0,1]
	s_mov_b64 s[14:15], 0x9d44000
	v_lshl_add_u64 v[8:9], v[20:21], 0, s[14:15]
	v_cvt_pk_bf16_f32 v6, v2, v3
	v_cvt_pk_bf16_f32 v7, v4, v5
	global_store_dwordx2 v[8:9], v[6:7], off sc1
	s_waitcnt vmcnt(15)
	v_mul_f32_e32 v72, 0x3fb8aa3b, v72
	v_exp_f32_e32 v10, v72
	v_lshlrev_b32_e32 v8, 16, v46
	v_and_b32_e32 v9, 0xffff0000, v46
	v_lshlrev_b32_e32 v32, 16, v47
	v_and_b32_e32 v33, 0xffff0000, v47
	v_pk_fma_f32 v[2:3], v[2:3], v[10:11], v[8:9] op_sel_hi:[1,0,1]
	v_pk_fma_f32 v[4:5], v[4:5], v[10:11], v[32:33] op_sel_hi:[1,0,1]
	s_mov_b64 s[14:15], 0x9d55000
	v_lshl_add_u64 v[8:9], v[20:21], 0, s[14:15]
	v_cvt_pk_bf16_f32 v6, v2, v3
	v_cvt_pk_bf16_f32 v7, v4, v5
	global_store_dwordx2 v[8:9], v[6:7], off sc1
	s_waitcnt vmcnt(15)
	v_mul_f32_e32 v73, 0x3fb8aa3b, v73
	v_exp_f32_e32 v10, v73
	v_lshlrev_b32_e32 v8, 16, v48
	v_and_b32_e32 v9, 0xffff0000, v48
	v_lshlrev_b32_e32 v32, 16, v49
	v_and_b32_e32 v33, 0xffff0000, v49
	v_pk_fma_f32 v[2:3], v[2:3], v[10:11], v[8:9] op_sel_hi:[1,0,1]
	v_pk_fma_f32 v[4:5], v[4:5], v[10:11], v[32:33] op_sel_hi:[1,0,1]
	s_mov_b64 s[14:15], 0x9d66000
	v_lshl_add_u64 v[8:9], v[20:21], 0, s[14:15]
	v_cvt_pk_bf16_f32 v6, v2, v3
	v_cvt_pk_bf16_f32 v7, v4, v5
	global_store_dwordx2 v[8:9], v[6:7], off sc1
	s_waitcnt vmcnt(15)
	v_mul_f32_e32 v74, 0x3fb8aa3b, v74
	v_exp_f32_e32 v10, v74
	v_lshlrev_b32_e32 v8, 16, v50
	v_and_b32_e32 v9, 0xffff0000, v50
	v_lshlrev_b32_e32 v32, 16, v51
	v_and_b32_e32 v33, 0xffff0000, v51
	v_pk_fma_f32 v[2:3], v[2:3], v[10:11], v[8:9] op_sel_hi:[1,0,1]
	v_pk_fma_f32 v[4:5], v[4:5], v[10:11], v[32:33] op_sel_hi:[1,0,1]
	s_mov_b64 s[14:15], 0x9d77000
	v_lshl_add_u64 v[8:9], v[20:21], 0, s[14:15]
	v_cvt_pk_bf16_f32 v6, v2, v3
	v_cvt_pk_bf16_f32 v7, v4, v5
	global_store_dwordx2 v[8:9], v[6:7], off sc1
	s_waitcnt vmcnt(15)
	v_mul_f32_e32 v75, 0x3fb8aa3b, v75
	v_exp_f32_e32 v10, v75
	v_lshlrev_b32_e32 v8, 16, v52
	v_and_b32_e32 v9, 0xffff0000, v52
	v_lshlrev_b32_e32 v32, 16, v53
	v_and_b32_e32 v33, 0xffff0000, v53
	v_pk_fma_f32 v[2:3], v[2:3], v[10:11], v[8:9] op_sel_hi:[1,0,1]
	v_pk_fma_f32 v[4:5], v[4:5], v[10:11], v[32:33] op_sel_hi:[1,0,1]
	s_mov_b64 s[14:15], 0x9d88000
	v_lshl_add_u64 v[8:9], v[20:21], 0, s[14:15]
	v_cvt_pk_bf16_f32 v6, v2, v3
	v_cvt_pk_bf16_f32 v7, v4, v5
	global_store_dwordx2 v[8:9], v[6:7], off sc1
	s_waitcnt vmcnt(15)
	v_mul_f32_e32 v76, 0x3fb8aa3b, v76
	v_exp_f32_e32 v10, v76
	v_lshlrev_b32_e32 v8, 16, v54
	v_and_b32_e32 v9, 0xffff0000, v54
	v_lshlrev_b32_e32 v32, 16, v55
	v_and_b32_e32 v33, 0xffff0000, v55
	v_pk_fma_f32 v[2:3], v[2:3], v[10:11], v[8:9] op_sel_hi:[1,0,1]
	v_pk_fma_f32 v[4:5], v[4:5], v[10:11], v[32:33] op_sel_hi:[1,0,1]
	s_mov_b64 s[14:15], 0x9d99000
	v_lshl_add_u64 v[8:9], v[20:21], 0, s[14:15]
	v_cvt_pk_bf16_f32 v6, v2, v3
	v_cvt_pk_bf16_f32 v7, v4, v5
	global_store_dwordx2 v[8:9], v[6:7], off sc1
	s_waitcnt vmcnt(15)
	v_mul_f32_e32 v77, 0x3fb8aa3b, v77
	v_exp_f32_e32 v10, v77
	v_lshlrev_b32_e32 v8, 16, v56
	v_and_b32_e32 v9, 0xffff0000, v56
	v_lshlrev_b32_e32 v32, 16, v57
	v_and_b32_e32 v33, 0xffff0000, v57
	v_pk_fma_f32 v[2:3], v[2:3], v[10:11], v[8:9] op_sel_hi:[1,0,1]
	v_pk_fma_f32 v[4:5], v[4:5], v[10:11], v[32:33] op_sel_hi:[1,0,1]
	s_mov_b64 s[14:15], 0x9daa000
	v_lshl_add_u64 v[8:9], v[20:21], 0, s[14:15]
	v_cvt_pk_bf16_f32 v6, v2, v3
	v_cvt_pk_bf16_f32 v7, v4, v5
	global_store_dwordx2 v[8:9], v[6:7], off sc1
	s_waitcnt vmcnt(15)
	v_mul_f32_e32 v78, 0x3fb8aa3b, v78
	v_exp_f32_e32 v10, v78
	v_lshlrev_b32_e32 v8, 16, v58
	v_and_b32_e32 v9, 0xffff0000, v58
	v_lshlrev_b32_e32 v32, 16, v59
	v_and_b32_e32 v33, 0xffff0000, v59
	v_pk_fma_f32 v[2:3], v[2:3], v[10:11], v[8:9] op_sel_hi:[1,0,1]
	v_pk_fma_f32 v[4:5], v[4:5], v[10:11], v[32:33] op_sel_hi:[1,0,1]
	s_mov_b64 s[14:15], 0x9dbb000
	v_lshl_add_u64 v[8:9], v[20:21], 0, s[14:15]
	v_cvt_pk_bf16_f32 v6, v2, v3
	v_cvt_pk_bf16_f32 v7, v4, v5
	global_store_dwordx2 v[8:9], v[6:7], off sc1
	s_waitcnt vmcnt(15)
	v_mul_f32_e32 v79, 0x3fb8aa3b, v79
	v_exp_f32_e32 v10, v79
	v_lshlrev_b32_e32 v8, 16, v60
	v_and_b32_e32 v9, 0xffff0000, v60
	v_lshlrev_b32_e32 v32, 16, v61
	v_and_b32_e32 v33, 0xffff0000, v61
	v_pk_fma_f32 v[2:3], v[2:3], v[10:11], v[8:9] op_sel_hi:[1,0,1]
	v_pk_fma_f32 v[4:5], v[4:5], v[10:11], v[32:33] op_sel_hi:[1,0,1]
	s_mov_b64 s[14:15], 0x9dcc000
	v_lshl_add_u64 v[8:9], v[20:21], 0, s[14:15]
	v_cvt_pk_bf16_f32 v6, v2, v3
	v_cvt_pk_bf16_f32 v7, v4, v5
	global_store_dwordx2 v[8:9], v[6:7], off sc1
	s_waitcnt vmcnt(15)
	v_mul_f32_e32 v80, 0x3fb8aa3b, v80
	v_exp_f32_e32 v10, v80
	v_lshlrev_b32_e32 v8, 16, v62
	v_and_b32_e32 v9, 0xffff0000, v62
	v_lshlrev_b32_e32 v32, 16, v63
	v_and_b32_e32 v33, 0xffff0000, v63
	v_pk_fma_f32 v[2:3], v[2:3], v[10:11], v[8:9] op_sel_hi:[1,0,1]
	v_pk_fma_f32 v[4:5], v[4:5], v[10:11], v[32:33] op_sel_hi:[1,0,1]
	s_mov_b64 s[14:15], 0x9ddd000
	v_lshl_add_u64 v[8:9], v[20:21], 0, s[14:15]
	v_cvt_pk_bf16_f32 v6, v2, v3
	v_cvt_pk_bf16_f32 v7, v4, v5
	global_store_dwordx2 v[8:9], v[6:7], off sc1
	s_waitcnt vmcnt(15)
	v_mul_f32_e32 v81, 0x3fb8aa3b, v81
	v_exp_f32_e32 v10, v81
	v_lshlrev_b32_e32 v8, 16, v64
	v_and_b32_e32 v9, 0xffff0000, v64
	v_lshlrev_b32_e32 v32, 16, v65
	v_and_b32_e32 v33, 0xffff0000, v65
	v_pk_fma_f32 v[2:3], v[2:3], v[10:11], v[8:9] op_sel_hi:[1,0,1]
	v_pk_fma_f32 v[4:5], v[4:5], v[10:11], v[32:33] op_sel_hi:[1,0,1]
	s_mov_b64 s[14:15], 0x9dee000
	v_lshl_add_u64 v[8:9], v[20:21], 0, s[14:15]
	v_cvt_pk_bf16_f32 v6, v2, v3
	v_cvt_pk_bf16_f32 v7, v4, v5
	global_store_dwordx2 v[8:9], v[6:7], off sc1
	s_waitcnt vmcnt(15)
	v_mul_f32_e32 v82, 0x3fb8aa3b, v82
	v_exp_f32_e32 v10, v82
	v_lshlrev_b32_e32 v8, 16, v66
	v_and_b32_e32 v9, 0xffff0000, v66
	v_lshlrev_b32_e32 v32, 16, v67
	v_and_b32_e32 v33, 0xffff0000, v67
	v_pk_fma_f32 v[2:3], v[2:3], v[10:11], v[8:9] op_sel_hi:[1,0,1]
	v_pk_fma_f32 v[4:5], v[4:5], v[10:11], v[32:33] op_sel_hi:[1,0,1]
	s_mov_b64 s[14:15], 0x9dff000
	v_lshl_add_u64 v[8:9], v[20:21], 0, s[14:15]
	v_cvt_pk_bf16_f32 v6, v2, v3
	v_cvt_pk_bf16_f32 v7, v4, v5
	global_store_dwordx2 v[8:9], v[6:7], off sc1
	s_mov_b64 s[14:15], 0x110000
	v_lshl_add_u64 v[16:17], v[16:17], 0, s[14:15]
	v_lshl_add_u64 v[18:19], v[18:19], 0, 64
	s_add_i32 s13, s13, 16
	s_cmp_eq_u32 s13, 32
	s_cbranch_scc0 .LBB0_485
	v_add_u32_e32 v1, s9, v1
	s_mov_b32 s13, 0x10fff
	v_cmp_lt_i32_e32 vcc, s13, v1
	s_or_b64 s[6:7], vcc, s[6:7]
	s_andn2_b64 exec, exec, s[6:7]
	s_cbranch_execnz .LBB0_484
